# baseline (speedup 1.0000x reference)
.Lk2f_w7:
	v_mov_b32_e32 v8, 0
	ds_read_b128 v[4:7], v8 offset:19216
	s_waitcnt lgkmcnt(0)
	v_max_u32_e32 v9, v14, v15
	v_cmp_lt_u32_e32 vcc, 32, v9
	s_cmp_lg_u64 vcc, 0
	s_cbranch_scc1 .Lk2f_fallback
	v_add3_u32 v4, v4, v5, v6
	v_add_u32_e32 v4, v4, v7
	v_add_u32_e32 v11, v14, v15
	s_nop 1
	v_add_u32_dpp v12, v11, v11 row_shr:1 row_mask:0xf bank_mask:0xf bound_ctrl:1
	s_nop 1
	v_add_u32_dpp v12, v12, v12 row_shr:2 row_mask:0xf bank_mask:0xf bound_ctrl:1
	s_nop 1
	v_add_u32_dpp v12, v12, v12 row_shr:4 row_mask:0xf bank_mask:0xf bound_ctrl:1
	s_nop 1
	v_add_u32_dpp v12, v12, v12 row_shr:8 row_mask:0xf bank_mask:0xf bound_ctrl:1
	s_nop 1
	v_add_u32_dpp v12, v12, v12 row_bcast:15 row_mask:0xa bank_mask:0xf
	s_nop 1
	v_add_u32_dpp v12, v12, v12 row_bcast:31 row_mask:0xc bank_mask:0xf
	v_sub_u32_e32 v12, v12, v11
	v_add_u32_e32 v12, v12, v4
	v_add_u32_e32 v13, v12, v14
	s_mul_i32 s6, s3, 0x62
	v_lshl_add_u32 v16, v1, 1, s6
	s_movk_i32 s7, 49
	v_cmp_gt_u32_e32 vcc, s7, v1
	s_mov_b32 s7, 0x186a0
	v_cmp_gt_u32_e64 s[38:39], s7, v16
	s_and_b64 vcc, vcc, s[38:39]
	v_lshlrev_b32_e32 v17, 2, v16
	s_and_saveexec_b64 s[40:41], vcc
	s_cbranch_execz .Lk2f_w7a
	global_store_dwordx2 v17, v[12:13], s[14:15] sc1
